# MoBA past-block step: ALiBi init under the fragment reads, second sub-tile K fragments prefetched during the first softmax
# baseline (speedup 1.0000x reference)
; __device__ __forceinline__ float max2_raw(float a, float b) { float d; asm("v_max_f32 %0, %1, %2" : "=v"(d) : "v"(a), "v"(b)); return d; }
; template <int MODE>
; __device__ __forceinline__ void attn_moba_sub(const bf16x8 (&qr)[4], f32x16& O0, f32x16& O1, float& m, float& l, unsigned saddr, int j, int kv0, int q, int q0, int hi, float slope2, bool rowok) {
;     bf16x8 kf[4], vf[2][2];
;     asm volatile("ds_read_b128 %0, %8\n\tds_read_b128 %1, %8 offset:1024\n\tds_read_b128 %2, %8 offset:2048\n\tds_read_b128 %3, %8 offset:3072\n\t"
;                  "ds_read_b128 %4, %9\n\tds_read_b128 %5, %9 offset:1024\n\tds_read_b128 %6, %9 offset:2048\n\tds_read_b128 %7, %9 offset:3072\n\ts_waitcnt lgkmcnt(0)"
;                  : "=&v"(kf[0]), "=&v"(kf[1]), "=&v"(kf[2]), "=&v"(kf[3]), "=&v"(vf[0][0]), "=&v"(vf[0][1]), "=&v"(vf[1][0]), "=&v"(vf[1][1])
;                  : "v"(saddr + (unsigned)j * 4096u), "v"(saddr + 8192u + (unsigned)j * 4096u) : "memory");
;     f32x16 S; const float sbase = slope2 * (float)(kv0 + 8 * hi - q0);
; #pragma unroll
;     for (int r = 0; r < 16; ++r) S[r] = sbase + slope2 * (float)((r & 7) + 16 * (r >> 3));
; #pragma unroll
;     for (int d0 = 0; d0 < 4; ++d0) S = __builtin_amdgcn_mfma_f32_32x32x16_bf16(kf[d0], qr[d0], S, 0, 0, 0);
;     if (MODE == 1) {
; #pragma unroll
;         for (int r = 0; r < 16; ++r) { const int key = kv0 + (r & 7) + 8 * hi + 16 * (r >> 3); if (key > q) S[r] = -INFINITY; }
;     }
;     if (MODE == 2) { if (!rowok) {
; #pragma unroll
;         for (int r = 0; r < 16; ++r) S[r] = -INFINITY; } }
;     float rm = rowmax16_raw(S);
;     { const auto rr = __builtin_amdgcn_permlane32_swap(__float_as_uint(rm), __float_as_uint(rm), false, false); rm = max2_raw(__uint_as_float(rr[0]), __uint_as_float(rr[1])); }
;     if (__any(rm > m)) { const float mn = fmaxf(fmaxf(m, rm), -1e30f); const float alpha = __builtin_amdgcn_exp2f(m - mn); l *= alpha; O0 *= alpha; O1 *= alpha; m = mn; }
.LBB0_1331:
	s_lshr_b32 s0, s92, 2
	s_lshl_b32 s0, 1, s0
	s_and_b32 s1, s0, s79
	s_cmp_eq_u32 s1, 0
	s_cbranch_scc1 .LBB0_1337
	v_add_u32_e32 v113, s89, v195
	s_nop 1
	v_add_u32_e32 v80, 0xe0, v113
	v_add_u32_e32 v229, 0x1000, v198
	v_add_u32_e32 v230, 0x3000, v198
	v_cvt_f32_i32_e32 v80, v80
	ds_read_b128 v[114:117], v229
	ds_read_b128 v[118:121], v229 offset:1024
	ds_read_b128 v[122:125], v229 offset:2048
	ds_read_b128 v[144:147], v229 offset:3072
	ds_read_b128 v[108:111], v230
	ds_read_b128 v[100:103], v230 offset:1024
	ds_read_b128 v[104:107], v230 offset:2048
	ds_read_b128 v[96:99], v230 offset:3072
	v_add_u32_e32 v228, 0x2000, v198
	v_and_b32_e32 v112, s0, v193
	v_cmp_eq_u32_e64 s[70:71], 0, v112
	v_mul_f32_e32 v80, v163, v80
	s_nop 0
	v_cndmask_b32_e64 v80, v80, v190, s[70:71]
	v_pk_add_f32 v[94:95], v[176:177], v[80:81] op_sel_hi:[1,0]
	v_pk_add_f32 v[92:93], v[174:175], v[80:81] op_sel_hi:[1,0]
	v_pk_add_f32 v[90:91], v[172:173], v[80:81] op_sel_hi:[1,0]
	v_pk_add_f32 v[88:89], v[170:171], v[80:81] op_sel_hi:[1,0]
	v_pk_add_f32 v[86:87], v[168:169], v[80:81] op_sel_hi:[1,0]
	v_pk_add_f32 v[84:85], v[166:167], v[80:81] op_sel_hi:[1,0]
	v_pk_add_f32 v[82:83], v[164:165], v[80:81] op_sel_hi:[1,0]
	v_pk_add_f32 v[80:81], v[162:163], v[80:81] op_sel_hi:[1,0]
	s_waitcnt lgkmcnt(4)
	s_nop 1
	v_mfma_f32_32x32x16_bf16 v[80:95], v[114:117], v[128:131], v[80:95]
	v_mfma_f32_32x32x16_bf16 v[80:95], v[118:121], v[132:135], v[80:95]
	v_mfma_f32_32x32x16_bf16 v[80:95], v[122:125], v[136:139], v[80:95]
	v_mfma_f32_32x32x16_bf16 v[80:95], v[144:147], v[140:143], v[80:95]
	ds_read_b128 v[114:117], v198
	ds_read_b128 v[118:121], v198 offset:1024
	ds_read_b128 v[122:125], v198 offset:2048
	ds_read_b128 v[144:147], v198 offset:3072
	s_nop 7
	v_max3_f32 v222, v80, v81, v82
	v_max3_f32 v223, v83, v84, v85
	v_max3_f32 v224, v86, v87, v88
	v_max3_f32 v222, v222, v223, v224
	v_max3_f32 v223, v89, v90, v91
	v_max3_f32 v224, v92, v93, v94
	v_max3_f32 v223, v223, v224, v95
	v_max_f32_e32 v222, v222, v223
	v_mov_b32_e32 v223, v222
	s_nop 1
	v_permlane32_swap_b32_e32 v222, v223
	v_max_f32_e32 v223, v222, v223
	v_cmp_gt_f32_e32 vcc, v223, v196
	s_cbranch_vccz .Lmoba_m2_1
	v_max3_f32 v227, v196, v223, s86
	v_sub_f32_e32 v226, v196, v227
	v_exp_f32_e32 v226, v226
	v_mov_b32_e32 v196, v227
	v_mul_f32_e32 v197, v197, v226
	v_pk_mul_f32 v[62:63], v[62:63], v[226:227] op_sel_hi:[1,0]
	v_pk_mul_f32 v[60:61], v[60:61], v[226:227] op_sel_hi:[1,0]
	v_pk_mul_f32 v[58:59], v[58:59], v[226:227] op_sel_hi:[1,0]
	v_pk_mul_f32 v[56:57], v[56:57], v[226:227] op_sel_hi:[1,0]
	v_pk_mul_f32 v[54:55], v[54:55], v[226:227] op_sel_hi:[1,0]
	v_pk_mul_f32 v[52:53], v[52:53], v[226:227] op_sel_hi:[1,0]
	v_pk_mul_f32 v[50:51], v[50:51], v[226:227] op_sel_hi:[1,0]
	v_pk_mul_f32 v[48:49], v[48:49], v[226:227] op_sel_hi:[1,0]
	v_pk_mul_f32 v[78:79], v[78:79], v[226:227] op_sel_hi:[1,0]
	v_pk_mul_f32 v[76:77], v[76:77], v[226:227] op_sel_hi:[1,0]
	v_pk_mul_f32 v[74:75], v[74:75], v[226:227] op_sel_hi:[1,0]
	v_pk_mul_f32 v[72:73], v[72:73], v[226:227] op_sel_hi:[1,0]
	v_pk_mul_f32 v[70:71], v[70:71], v[226:227] op_sel_hi:[1,0]
	v_pk_mul_f32 v[68:69], v[68:69], v[226:227] op_sel_hi:[1,0]
	v_pk_mul_f32 v[66:67], v[66:67], v[226:227] op_sel_hi:[1,0]
	v_pk_mul_f32 v[64:65], v[64:65], v[226:227] op_sel_hi:[1,0]
; __device__ __forceinline__ unsigned pk2(float lo, float hi) { const f32x2_pk v = {lo, hi}; return __builtin_bit_cast(unsigned, __builtin_convertvector(v, bf16x2)); }
; template <int MODE>
; __device__ __forceinline__ void attn_moba_sub(const bf16x8 (&qr)[4], f32x16& O0, f32x16& O1, float& m, float& l, unsigned saddr, int j, int kv0, int q, int q0, int hi, float slope2, bool rowok) {
;     ...
;     if (__any(rm > m)) { const float mn = fmaxf(fmaxf(m, rm), -1e30f); const float alpha = __builtin_amdgcn_exp2f(m - mn); l *= alpha; O0 *= alpha; O1 *= alpha; m = mn; }
;     float p[16]; float ps = 0.f;
; #pragma unroll
;     for (int r = 0; r < 16; ++r) { p[r] = __builtin_amdgcn_exp2f(S[r] - m); ps += p[r]; }
;     l += ps;
;     u32x4 w0, w1;
;     w0.x = pk2(p[0], p[1]); w0.y = pk2(p[2], p[3]); w0.z = pk2(p[4], p[5]); w0.w = pk2(p[6], p[7]);
;     w1.x = pk2(p[8], p[9]); w1.y = pk2(p[10], p[11]); w1.z = pk2(p[12], p[13]); w1.w = pk2(p[14], p[15]);
;     const bf16x8 pf0 = __builtin_bit_cast(bf16x8, w0), pf1 = __builtin_bit_cast(bf16x8, w1);
;     O0 = __builtin_amdgcn_mfma_f32_32x32x16_bf16(vf[0][0], pf0, O0, 0, 0, 0); O0 = __builtin_amdgcn_mfma_f32_32x32x16_bf16(vf[1][0], pf1, O0, 0, 0, 0);
;     O1 = __builtin_amdgcn_mfma_f32_32x32x16_bf16(vf[0][1], pf0, O1, 0, 0, 0); O1 = __builtin_amdgcn_mfma_f32_32x32x16_bf16(vf[1][1], pf1, O1, 0, 0, 0);
.Lmoba_m2_1:
	v_sub_f32_e32 v80, v80, v196
	v_exp_f32_e32 v80, v80
	v_sub_f32_e32 v81, v81, v196
	v_exp_f32_e32 v81, v81
	v_sub_f32_e32 v82, v82, v196
	v_exp_f32_e32 v82, v82
	v_sub_f32_e32 v83, v83, v196
	v_exp_f32_e32 v83, v83
	v_add_f32_e32 v225, 0, v80
	v_sub_f32_e32 v84, v84, v196
	v_exp_f32_e32 v84, v84
	v_add_f32_e32 v225, v81, v225
	v_sub_f32_e32 v85, v85, v196
	v_exp_f32_e32 v85, v85
	v_add_f32_e32 v225, v82, v225
	v_sub_f32_e32 v86, v86, v196
	v_exp_f32_e32 v86, v86
	v_add_f32_e32 v225, v83, v225
	v_sub_f32_e32 v87, v87, v196
	v_exp_f32_e32 v87, v87
	v_add_f32_e32 v225, v84, v225
	v_sub_f32_e32 v88, v88, v196
	v_exp_f32_e32 v88, v88
	v_add_f32_e32 v225, v85, v225
	v_sub_f32_e32 v89, v89, v196
	v_exp_f32_e32 v89, v89
	v_add_f32_e32 v225, v86, v225
	v_sub_f32_e32 v90, v90, v196
	v_exp_f32_e32 v90, v90
	v_add_f32_e32 v225, v87, v225
	v_sub_f32_e32 v91, v91, v196
	v_exp_f32_e32 v91, v91
	v_cvt_pk_bf16_f32 v80, v80, v81
	v_cvt_pk_bf16_f32 v81, v82, v83
	v_cvt_pk_bf16_f32 v82, v84, v85
	v_cvt_pk_bf16_f32 v83, v86, v87
	v_add_f32_e32 v225, v88, v225
	v_sub_f32_e32 v92, v92, v196
	v_exp_f32_e32 v92, v92
	s_waitcnt lgkmcnt(4)
	v_mfma_f32_32x32x16_bf16 v[48:63], v[108:111], v[80:83], v[48:63]
	v_add_f32_e32 v225, v89, v225
	v_sub_f32_e32 v93, v93, v196
	v_exp_f32_e32 v93, v93
	v_add_f32_e32 v225, v90, v225
	v_sub_f32_e32 v94, v94, v196
	v_exp_f32_e32 v94, v94
	v_add_f32_e32 v225, v91, v225
	v_sub_f32_e32 v95, v95, v196
	v_exp_f32_e32 v95, v95
	v_mfma_f32_32x32x16_bf16 v[64:79], v[100:103], v[80:83], v[64:79]
	v_add_f32_e32 v225, v92, v225
	v_add_f32_e32 v225, v93, v225
	v_add_f32_e32 v225, v94, v225
	v_add_f32_e32 v225, v95, v225
	v_cvt_pk_bf16_f32 v84, v88, v89
	v_cvt_pk_bf16_f32 v85, v90, v91
	v_cvt_pk_bf16_f32 v86, v92, v93
	v_cvt_pk_bf16_f32 v87, v94, v95
	v_add_f32_e32 v112, v197, v225
	s_nop 0
	v_mfma_f32_32x32x16_bf16 v[48:63], v[104:107], v[84:87], v[48:63]
	v_mfma_f32_32x32x16_bf16 v[64:79], v[96:99], v[84:87], v[64:79]
	ds_read_b128 v[108:111], v228
	ds_read_b128 v[100:103], v228 offset:1024
	ds_read_b128 v[104:107], v228 offset:2048
	ds_read_b128 v[96:99], v228 offset:3072
	v_add_u32_e32 v80, 0xc0, v113
	v_cvt_f32_i32_e32 v80, v80
	v_mul_f32_e32 v80, v163, v80
	v_cndmask_b32_e64 v80, v80, v190, s[70:71]
	v_pk_add_f32 v[94:95], v[176:177], v[80:81] op_sel_hi:[1,0]
	v_pk_add_f32 v[92:93], v[174:175], v[80:81] op_sel_hi:[1,0]
	v_pk_add_f32 v[90:91], v[172:173], v[80:81] op_sel_hi:[1,0]
	v_pk_add_f32 v[88:89], v[170:171], v[80:81] op_sel_hi:[1,0]
	v_pk_add_f32 v[86:87], v[168:169], v[80:81] op_sel_hi:[1,0]
	v_pk_add_f32 v[84:85], v[166:167], v[80:81] op_sel_hi:[1,0]
	v_pk_add_f32 v[82:83], v[164:165], v[80:81] op_sel_hi:[1,0]
	v_pk_add_f32 v[80:81], v[162:163], v[80:81] op_sel_hi:[1,0]
	s_waitcnt lgkmcnt(4)
	s_nop 1
	v_mfma_f32_32x32x16_bf16 v[80:95], v[114:117], v[128:131], v[80:95]
	v_mfma_f32_32x32x16_bf16 v[80:95], v[118:121], v[132:135], v[80:95]
	v_mfma_f32_32x32x16_bf16 v[80:95], v[122:125], v[136:139], v[80:95]
	v_mfma_f32_32x32x16_bf16 v[80:95], v[144:147], v[140:143], v[80:95]
	s_nop 11
	v_max3_f32 v222, v80, v81, v82
	v_max3_f32 v223, v83, v84, v85
	v_max3_f32 v224, v86, v87, v88
	v_max3_f32 v222, v222, v223, v224
	v_max3_f32 v223, v89, v90, v91
	v_max3_f32 v224, v92, v93, v94
	v_max3_f32 v223, v223, v224, v95
	v_max_f32_e32 v222, v222, v223
	v_mov_b32_e32 v223, v222
	s_nop 1
	v_permlane32_swap_b32_e32 v222, v223
	v_max_f32_e32 v223, v222, v223
	v_cmp_gt_f32_e32 vcc, v223, v196
	s_cbranch_vccz .Lmoba_m2_2
	v_max3_f32 v227, v196, v223, s86
	v_sub_f32_e32 v226, v196, v227
	v_exp_f32_e32 v226, v226
	v_mov_b32_e32 v196, v227
	v_mul_f32_e32 v112, v226, v112
	v_pk_mul_f32 v[62:63], v[62:63], v[226:227] op_sel_hi:[1,0]
	v_pk_mul_f32 v[60:61], v[60:61], v[226:227] op_sel_hi:[1,0]
	v_pk_mul_f32 v[58:59], v[58:59], v[226:227] op_sel_hi:[1,0]
	v_pk_mul_f32 v[56:57], v[56:57], v[226:227] op_sel_hi:[1,0]
	v_pk_mul_f32 v[54:55], v[54:55], v[226:227] op_sel_hi:[1,0]
	v_pk_mul_f32 v[52:53], v[52:53], v[226:227] op_sel_hi:[1,0]
	v_pk_mul_f32 v[50:51], v[50:51], v[226:227] op_sel_hi:[1,0]
	v_pk_mul_f32 v[48:49], v[48:49], v[226:227] op_sel_hi:[1,0]
	v_pk_mul_f32 v[78:79], v[78:79], v[226:227] op_sel_hi:[1,0]
	v_pk_mul_f32 v[76:77], v[76:77], v[226:227] op_sel_hi:[1,0]
	v_pk_mul_f32 v[74:75], v[74:75], v[226:227] op_sel_hi:[1,0]
	v_pk_mul_f32 v[72:73], v[72:73], v[226:227] op_sel_hi:[1,0]
	v_pk_mul_f32 v[70:71], v[70:71], v[226:227] op_sel_hi:[1,0]
	v_pk_mul_f32 v[68:69], v[68:69], v[226:227] op_sel_hi:[1,0]
	v_pk_mul_f32 v[66:67], v[66:67], v[226:227] op_sel_hi:[1,0]
	v_pk_mul_f32 v[64:65], v[64:65], v[226:227] op_sel_hi:[1,0]
.Lmoba_m2_2:
	v_sub_f32_e32 v80, v80, v196
	v_exp_f32_e32 v80, v80
	v_sub_f32_e32 v81, v81, v196
	v_exp_f32_e32 v81, v81
	v_sub_f32_e32 v82, v82, v196
	v_exp_f32_e32 v82, v82
	v_sub_f32_e32 v83, v83, v196
	v_exp_f32_e32 v83, v83
	v_add_f32_e32 v225, 0, v80
	v_sub_f32_e32 v84, v84, v196
	v_exp_f32_e32 v84, v84
	v_add_f32_e32 v225, v81, v225
	v_sub_f32_e32 v85, v85, v196
	v_exp_f32_e32 v85, v85
	v_add_f32_e32 v225, v82, v225
	v_sub_f32_e32 v86, v86, v196
	v_exp_f32_e32 v86, v86
	v_add_f32_e32 v225, v83, v225
	v_sub_f32_e32 v87, v87, v196
	v_exp_f32_e32 v87, v87
	v_add_f32_e32 v225, v84, v225
	v_sub_f32_e32 v88, v88, v196
	v_exp_f32_e32 v88, v88
	v_add_f32_e32 v225, v85, v225
	v_sub_f32_e32 v89, v89, v196
	v_exp_f32_e32 v89, v89
	v_add_f32_e32 v225, v86, v225
	v_sub_f32_e32 v90, v90, v196
	v_exp_f32_e32 v90, v90
	v_add_f32_e32 v225, v87, v225
	v_sub_f32_e32 v91, v91, v196
	v_exp_f32_e32 v91, v91
	v_cvt_pk_bf16_f32 v80, v80, v81
	v_cvt_pk_bf16_f32 v81, v82, v83
	v_cvt_pk_bf16_f32 v82, v84, v85
	v_cvt_pk_bf16_f32 v83, v86, v87
	v_add_f32_e32 v225, v88, v225
	v_sub_f32_e32 v92, v92, v196
	v_exp_f32_e32 v92, v92
	s_waitcnt lgkmcnt(0)
	v_mfma_f32_32x32x16_bf16 v[48:63], v[108:111], v[80:83], v[48:63]
	v_add_f32_e32 v225, v89, v225
	v_sub_f32_e32 v93, v93, v196
	v_exp_f32_e32 v93, v93
	v_add_f32_e32 v225, v90, v225
	v_sub_f32_e32 v94, v94, v196
	v_exp_f32_e32 v94, v94
	v_add_f32_e32 v225, v91, v225
	v_sub_f32_e32 v95, v95, v196
	v_exp_f32_e32 v95, v95
	v_mfma_f32_32x32x16_bf16 v[64:79], v[100:103], v[80:83], v[64:79]
	v_add_f32_e32 v225, v92, v225
	v_add_f32_e32 v225, v93, v225
	v_add_f32_e32 v225, v94, v225
	v_add_f32_e32 v225, v95, v225
	v_cvt_pk_bf16_f32 v84, v88, v89
	v_cvt_pk_bf16_f32 v85, v90, v91
	v_cvt_pk_bf16_f32 v86, v92, v93
	v_cvt_pk_bf16_f32 v87, v94, v95
	v_add_f32_e32 v197, v112, v225
	s_nop 0
	v_mfma_f32_32x32x16_bf16 v[48:63], v[104:107], v[84:87], v[48:63]
	v_mfma_f32_32x32x16_bf16 v[64:79], v[96:99], v[84:87], v[64:79]
